# indexer work-queue ticket drawn one unit ahead (atomic round trip off the unit head)
# speedup vs baseline: 1.0075x; 1.0075x over previous
.LBB0_1222:
	v_readlane_b32 s0, v253, 38
	s_lshl_b32 s80, s0, 6
	s_lshl_b64 s[0:1], s[80:81], 2
	s_add_u32 s0, s74, s0
	s_addc_u32 s1, s75, s1
	s_add_u32 s0, s0, 0x1000
	s_addc_u32 s1, s1, 0
	v_writelane_b32 v253, s0, 53
	s_waitcnt vmcnt(0) lgkmcnt(0)
	s_barrier
	v_writelane_b32 v253, s1, 54
	s_nop 0
	v_readlane_b32 s0, v253, 32
	v_readlane_b32 s1, v253, 33
	s_nop 0
	v_or_b32_e32 v0, s0, v198
	v_cmp_eq_u32_e64 s[36:37], 0, v0
	s_and_saveexec_b64 s[0:1], s[36:37]
	s_cbranch_execz .LBB0_1226
	s_mov_b64 s[16:17], exec
	v_mbcnt_lo_u32_b32 v0, s16, 0
	v_mbcnt_hi_u32_b32 v0, s17, v0
	v_cmp_eq_u32_e32 vcc, 0, v0
	s_and_saveexec_b64 s[14:15], vcc
	s_cbranch_execz .LBB0_1225
	s_bcnt1_i32_b64 s16, s[16:17]
	v_mov_b32_e32 v2, s16
	v_readlane_b32 s16, v253, 53
	v_readlane_b32 s17, v253, 54
	s_nop 4
	global_atomic_add v2, v1, v2, s[16:17] sc0
	global_atomic_add v229, v1, v225, s[16:17] sc0

.LBB0_1231:
	s_waitcnt lgkmcnt(1)
	v_mov_b32_e32 v0, 0
	s_and_saveexec_b64 s[40:41], s[36:37]
	s_cbranch_execz .LBB0_1235
	s_waitcnt vmcnt(0) lgkmcnt(0)
	v_mov_b32_e32 v0, v229

.LBB0_1252:
	s_or_b64 exec, exec, s[40:41]
	s_lshl_b32 s17, s17, 2
	s_or_b32 s17, s17, 0x20420
	s_waitcnt lgkmcnt(0)
	s_barrier
	s_and_saveexec_b64 s[42:43], s[36:37]
	s_cbranch_execz .Ltk_ahead_skip
	v_readlane_b32 s44, v253, 53
	v_readlane_b32 s45, v253, 54
	s_nop 4
	global_atomic_add v229, v1, v225, s[44:45] sc0
.Ltk_ahead_skip:
	s_or_b64 exec, exec, s[42:43]
	v_mov_b32_e32 v0, s17
	ds_read_b32 v0, v0
	s_movk_i32 s29, 0xfff
	s_waitcnt lgkmcnt(0)
	v_cmp_lt_u32_e64 s[40:41], s29, v0
	v_readfirstlane_b32 s17, v0
	s_and_b64 vcc, exec, s[40:41]
	s_cbranch_vccnz .LBB0_1256
	s_not_b32 s29, s17
	s_lshl_b32 s29, s29, 1
	s_lshl_b32 s43, s17, 13
	s_and_b32 s42, s29, 0x1ffc
	s_and_b32 s43, s43, 0x2000
	s_or_b32 s42, s42, s43
	v_or_b32_e32 v0, s42, v143
	v_lshlrev_b32_e32 v0, 10, v0
	s_bfe_u32 s29, s29, 0x80005
	v_readlane_b32 s44, v253, 32
	v_lshl_add_u64 v[2:3], v[102:103], 0, v[0:1]
	v_or_b32_e32 v0, s42, v140
	s_min_i32 s42, s44, s29
	v_readlane_b32 s44, v253, 31
	s_min_i32 s29, s44, s29
	s_lshr_b32 s44, s43, 5
	s_ashr_i32 s43, s42, 31
	s_add_u32 s42, s42, s44
	s_addc_u32 s43, s43, 0
	s_lshl_b64 s[42:43], s[42:43], 12
	global_load_dwordx4 v[18:21], v[2:3], off
	global_load_dwordx4 v[26:29], v[2:3], off offset:32
	global_load_dwordx4 v[30:33], v[2:3], off offset:64
	global_load_dwordx4 v[34:37], v[2:3], off offset:96
	v_lshl_add_u64 v[2:3], v[100:101], 0, s[42:43]
	s_ashr_i32 s43, s29, 31
	s_add_u32 s42, s29, s44
	s_addc_u32 s43, s43, 0
	v_lshlrev_b32_e32 v0, 5, v0
	s_lshl_b64 s[42:43], s[42:43], 12
	global_load_dwordx4 v[22:25], v0, s[82:83]
	global_load_dwordx4 v[38:41], v0, s[82:83] offset:16
	global_load_dwordx4 v[42:45], v0, s[82:83] offset:64
	global_load_dwordx4 v[46:49], v0, s[82:83] offset:80
	v_lshl_add_u64 v[4:5], v[100:101], 0, s[42:43]
	global_load_dwordx4 v[50:53], v[2:3], off
	global_load_dwordx4 v[62:65], v[2:3], off offset:1024
	global_load_dwordx4 v[78:81], v[4:5], off
	global_load_dwordx4 v[70:73], v[4:5], off offset:1024
	global_load_dwordx4 v[58:61], v[2:3], off offset:2048
	global_load_dwordx4 v[54:57], v[2:3], off offset:3072
	global_load_dwordx4 v[74:77], v[4:5], off offset:2048
	global_load_dwordx4 v[66:69], v[4:5], off offset:3072
	v_readlane_b32 s45, v253, 33
	s_cmpk_lt_u32 s34, 0x100
	v_mov_b32_e32 v149, 1
	s_cbranch_scc0 .LBB0_1257

.LBB0_1988:
	s_waitcnt vmcnt(0)
	s_mov_b64 s[0:1], 0
